# global attention unit prologue: tile-1 and tile-2 K/V loads issued together with the Q and tile-0 loads, tile 1 staged into LDS before the first barrier
# speedup vs baseline: 1.0025x; 1.0004x over previous
.LBB0_591:
	global_load_dwordx4 v[140:143], v[150:151], off
	global_load_dwordx4 v[136:139], v[150:151], off offset:32
	global_load_dwordx4 v[132:135], v[150:151], off offset:64
	global_load_dwordx4 v[128:131], v[150:151], off offset:96
	global_load_dwordx4 v[124:127], v[150:151], off offset:128
	global_load_dwordx4 v[120:123], v[150:151], off offset:160
	global_load_dwordx4 v[116:119], v[150:151], off offset:192
	global_load_dwordx4 v[112:115], v[150:151], off offset:224
	global_load_dwordx4 v[0:3], v[152:153], off
	global_load_dwordx4 v[4:7], v[154:155], off
	global_load_dwordx4 v[8:11], v[156:157], off
	global_load_dwordx4 v[12:15], v[158:159], off
	s_add_u32 s10, s6, 0x90000
	s_addc_u32 s11, s7, 0
	s_add_u32 s22, s8, 0x90000
	s_addc_u32 s23, s9, 0
	s_add_u32 s6, s6, 0x120000
	s_addc_u32 s7, s7, 0
	s_add_u32 s8, s8, 0x120000
	s_addc_u32 s9, s9, 0
	v_lshl_add_u64 v[96:97], s[22:23], 0, v[192:193]
	v_lshl_add_u64 v[98:99], s[22:23], 0, v[148:149]
	v_lshl_add_u64 v[100:101], s[10:11], 0, v[192:193]
	v_lshl_add_u64 v[102:103], s[10:11], 0, v[148:149]
	v_lshl_add_u64 v[104:105], s[8:9], 0, v[192:193]
	v_lshl_add_u64 v[106:107], s[8:9], 0, v[148:149]
	v_lshl_add_u64 v[108:109], s[6:7], 0, v[192:193]
	v_lshl_add_u64 v[110:111], s[6:7], 0, v[148:149]
	global_load_dwordx4 v[80:83], v[96:97], off
	global_load_dwordx4 v[84:87], v[98:99], off
	global_load_dwordx4 v[88:91], v[100:101], off
	global_load_dwordx4 v[92:95], v[102:103], off
	global_load_dwordx4 v[144:147], v[104:105], off
	global_load_dwordx4 v[152:155], v[106:107], off
	global_load_dwordx4 v[148:151], v[108:109], off
	global_load_dwordx4 v[156:159], v[110:111], off
	s_cmp_lg_u32 0, -1
	v_mov_b32_e32 v183, 0
	v_mov_b32_e32 v194, 0x8000
	v_mov_b32_e32 v216, 0xc000
	v_mov_b32_e32 v187, v193
	v_mov_b32_e32 v24, v183
	v_mov_b32_e32 v25, v183
	v_mov_b32_e32 v26, v183
	v_mov_b32_e32 v27, v183
	v_mov_b32_e32 v28, v183
	v_mov_b32_e32 v29, v183
	v_mov_b32_e32 v30, v183
	v_mov_b32_e32 v31, v183
	v_mov_b32_e32 v32, 0
	v_mov_b32_e32 v33, v183
	v_mov_b32_e32 v34, v183
	v_mov_b32_e32 v35, v183
	v_mov_b32_e32 v36, v183
	v_mov_b32_e32 v37, v183
	v_mov_b32_e32 v38, v183
	v_mov_b32_e32 v39, v183
	v_mov_b32_e32 v40, v183
	v_mov_b32_e32 v41, v183
	v_mov_b32_e32 v42, v183
	v_mov_b32_e32 v43, v183
	v_mov_b32_e32 v44, v183
	v_mov_b32_e32 v45, v183
	v_mov_b32_e32 v46, v183
	v_mov_b32_e32 v47, v183
	v_mov_b32_e32 v48, 0
	v_mov_b32_e32 v49, v183
	v_mov_b32_e32 v50, v183
	v_mov_b32_e32 v51, v183
	v_mov_b32_e32 v52, v183
	v_mov_b32_e32 v53, v183
	v_mov_b32_e32 v54, v183
	v_mov_b32_e32 v55, v183
	v_mov_b32_e32 v56, v183
	v_mov_b32_e32 v57, v183
	v_mov_b32_e32 v58, v183
	v_mov_b32_e32 v59, v183
	v_mov_b32_e32 v60, v183
	v_mov_b32_e32 v61, v183
	v_mov_b32_e32 v62, v183
	v_mov_b32_e32 v63, v183
	s_waitcnt vmcnt(11)
	ds_write_b128 v204, v[0:3]
	s_waitcnt vmcnt(10)
	ds_write_b128 v205, v[4:7]
	s_waitcnt vmcnt(9)
	ds_write_b128 v206, v[8:11] offset:32768
	s_waitcnt vmcnt(8)
	ds_write_b128 v207, v[12:15] offset:32768
	s_waitcnt vmcnt(7)
	ds_write_b128 v204, v[80:83] offset:16384
	s_waitcnt vmcnt(6)
	ds_write_b128 v205, v[84:87] offset:16384
	s_waitcnt vmcnt(5)
	ds_write_b128 v206, v[88:91] offset:49152
	s_waitcnt vmcnt(4)
	ds_write_b128 v207, v[92:95] offset:49152
	v_bitop3_b32 v0, v184, v175, v188 bitop3:0xde
	v_add_u32_e32 v212, 0, v0
	s_waitcnt lgkmcnt(0)
	s_barrier
	ds_read_b128 v[0:3], v212 offset:32768
	ds_read_b128 v[16:19], v212 offset:40960
	s_waitcnt lgkmcnt(1)
	v_mfma_f32_32x32x16_bf16 v[0:15], v[0:3], v[140:143], 0
	s_waitcnt lgkmcnt(0)
	v_mfma_f32_32x32x16_bf16 v[64:79], v[16:19], v[140:143], 0
	v_bitop3_b32 v16, v211, v175, v188 bitop3:0xde
	v_add_u32_e32 v211, 0, v16
	ds_read_b128 v[16:19], v211 offset:32768
	ds_read_b128 v[20:23], v211 offset:40960
	s_waitcnt lgkmcnt(1)
	v_mfma_f32_32x32x16_bf16 v[0:15], v[16:19], v[136:139], v[0:15]
	v_bitop3_b32 v16, v210, v175, v188 bitop3:0xde
	v_add_u32_e32 v210, 0, v16
	s_waitcnt lgkmcnt(0)
	v_mfma_f32_32x32x16_bf16 v[64:79], v[20:23], v[136:139], v[64:79]
	ds_read_b128 v[16:19], v210 offset:32768
	ds_read_b128 v[20:23], v210 offset:40960
	s_waitcnt lgkmcnt(1)
	v_mfma_f32_32x32x16_bf16 v[0:15], v[16:19], v[132:135], v[0:15]
	v_bitop3_b32 v16, v209, v175, v188 bitop3:0xde
	v_add_u32_e32 v209, 0, v16
	s_waitcnt lgkmcnt(0)
	v_mfma_f32_32x32x16_bf16 v[64:79], v[20:23], v[132:135], v[64:79]
	ds_read_b128 v[16:19], v209 offset:32768
	ds_read_b128 v[20:23], v209 offset:40960
	s_waitcnt lgkmcnt(1)
	v_mfma_f32_32x32x16_bf16 v[0:15], v[16:19], v[128:131], v[0:15]
	v_bitop3_b32 v16, v208, v175, v188 bitop3:0xde
	v_add_u32_e32 v208, 0, v16
	s_waitcnt lgkmcnt(0)
	v_mfma_f32_32x32x16_bf16 v[64:79], v[20:23], v[128:131], v[64:79]
	ds_read_b128 v[16:19], v208 offset:32768
	ds_read_b128 v[20:23], v208 offset:40960
	s_waitcnt lgkmcnt(1)
	v_mfma_f32_32x32x16_bf16 v[0:15], v[16:19], v[124:127], v[0:15]
	v_bitop3_b32 v16, v191, v175, v188 bitop3:0xde
	v_add_u32_e32 v213, 0, v16
	s_waitcnt lgkmcnt(0)
	v_mfma_f32_32x32x16_bf16 v[64:79], v[20:23], v[124:127], v[64:79]
	ds_read_b128 v[16:19], v213 offset:32768
	ds_read_b128 v[20:23], v213 offset:40960
	s_waitcnt lgkmcnt(1)
	v_mfma_f32_32x32x16_bf16 v[0:15], v[16:19], v[120:123], v[0:15]
	v_bitop3_b32 v16, v190, v175, v188 bitop3:0xde
	v_add_u32_e32 v214, 0, v16
	s_waitcnt lgkmcnt(0)
	v_mfma_f32_32x32x16_bf16 v[64:79], v[20:23], v[120:123], v[64:79]
	ds_read_b128 v[16:19], v214 offset:32768
	ds_read_b128 v[20:23], v214 offset:40960
	s_waitcnt lgkmcnt(1)
	v_mfma_f32_32x32x16_bf16 v[0:15], v[16:19], v[116:119], v[0:15]
	v_bitop3_b32 v16, v189, v175, v188 bitop3:0xde
	v_add_u32_e32 v215, 0, v16
	s_waitcnt lgkmcnt(0)
	v_mfma_f32_32x32x16_bf16 v[64:79], v[20:23], v[116:119], v[64:79]
	ds_read_b128 v[16:19], v215 offset:32768
	ds_read_b128 v[20:23], v215 offset:40960
	s_waitcnt lgkmcnt(1)
	v_mfma_f32_32x32x16_bf16 v[0:15], v[16:19], v[112:115], v[0:15]
	s_mov_b32 s8, 1
	s_waitcnt lgkmcnt(0)
	v_mfma_f32_32x32x16_bf16 v[64:79], v[20:23], v[112:115], v[64:79]
	s_nop 6
	v_exp_f32_e32 v231, v0
	v_exp_f32_e32 v233, v1
	v_exp_f32_e32 v228, v4
	v_exp_f32_e32 v230, v5
	v_exp_f32_e32 v223, v8
	v_exp_f32_e32 v225, v9
	v_exp_f32_e32 v188, v12
	v_exp_f32_e32 v191, v13
	v_exp_f32_e32 v229, v2
	v_exp_f32_e32 v232, v3
	v_exp_f32_e32 v226, v6
	v_exp_f32_e32 v227, v7
	v_exp_f32_e32 v222, v10
	v_exp_f32_e32 v224, v11
	v_exp_f32_e32 v189, v14
	v_exp_f32_e32 v190, v15
	s_cselect_b32 s6, 0, 0
	s_nop 0
	s_addk_i32 s6, 0x4000
	v_add_u32_e32 v177, s6, v174
	v_readlane_b32 s6, v254, 39
	s_add_u32 s2, s6, s2
	v_readlane_b32 s6, v254, 40
	s_addc_u32 s3, s6, s3
	v_add_u32_e32 v192, 0x48000, v186
	v_mov_b32_e32 v0, 0
	v_mov_b32_e32 v1, v183
	v_mov_b32_e32 v2, v183
	v_mov_b32_e32 v3, v183
	v_mov_b32_e32 v4, v183
	v_mov_b32_e32 v5, v183
	v_mov_b32_e32 v6, v183
	v_mov_b32_e32 v7, v183
	v_mov_b32_e32 v8, v183
	v_mov_b32_e32 v9, v183
	v_mov_b32_e32 v10, v183
	v_mov_b32_e32 v11, v183
	v_mov_b32_e32 v12, v183
	v_mov_b32_e32 v13, v183
	v_mov_b32_e32 v14, v183
	v_mov_b32_e32 v15, v183
	v_mov_b32_e32 v16, 0
	v_mov_b32_e32 v17, v183
	v_mov_b32_e32 v18, v183
	v_mov_b32_e32 v19, v183
	v_mov_b32_e32 v20, v183
	v_mov_b32_e32 v21, v183
	v_mov_b32_e32 v22, v183
	v_mov_b32_e32 v23, v183
	s_waitcnt lgkmcnt(0)
	s_barrier
	v_lshl_add_u64 v[196:197], s[2:3], 0, v[186:187]
	v_lshl_add_u64 v[198:199], s[2:3], 0, v[192:193]
	s_mov_b64 s[100:101], 0x11921000
	v_lshl_add_u64 v[196:197], v[196:197], 0, s[100:101]
	v_lshl_add_u64 v[198:199], v[198:199], 0, s[100:101]
	s_mov_b64 s[100:101], 0x90000
	s_branch .LBB0_593
